# P4 bisection count: 18/13/9/4 of 32/24/16/8 keys counted on the scalar unit (v_cmp->sgpr, s_bcnt1), rest v_cmp/v_addc; same counts
# speedup vs baseline: 1.0007x; 1.0007x over previous
; template <int NVM> __device__ __forceinline__ int cnt_ge(const unsigned (&key)[32], unsigned cand) {
;     unsigned c0 = 0, c1 = 0, c2 = 0, c3 = 0;
; #pragma unroll
;     for (int i = 0; i < NVM; i += 4) {
;         asm("v_cmp_ge_u32 vcc, %1, %2\n\tv_addc_co_u32 %0, vcc, 0, %0, vcc" : "+v"(c0) : "v"(key[i]), "v"(cand) : "vcc");
;         asm("v_cmp_ge_u32 vcc, %1, %2\n\tv_addc_co_u32 %0, vcc, 0, %0, vcc" : "+v"(c1) : "v"(key[i + 1]), "v"(cand) : "vcc");
;         asm("v_cmp_ge_u32 vcc, %1, %2\n\tv_addc_co_u32 %0, vcc, 0, %0, vcc" : "+v"(c2) : "v"(key[i + 2]), "v"(cand) : "vcc");
;         asm("v_cmp_ge_u32 vcc, %1, %2\n\tv_addc_co_u32 %0, vcc, 0, %0, vcc" : "+v"(c3) : "v"(key[i + 3]), "v"(cand) : "vcc"); }
;     const unsigned c = (c0 + c1) + (c2 + c3);
;     int tot = 0;
; #pragma unroll
;     for (int b = 0; b < 6; ++b) tot += __builtin_popcountll(__ballot((c >> b) & 1u)) << b;
;     return tot;
; }
; template <int NVM> __device__ __forceinline__ unsigned sel_thr(const unsigned (&key)[32]) {
;     unsigned Tt = 0u;
;     ...
;         if (cnt >= TOPK) { Tt = cand; if (cnt == TOPK) break; } }
;     return Tt;
; }
.LBB0_705:
	v_lshlrev_b32_e64 v85, v84, 1
	v_or_b32_e32 v85, v85, v66
	v_mov_b32_e32 v86, 0
	v_mov_b32_e32 v87, 0
	s_mov_b32 s12, 0
	v_cmp_ge_u32_e64 s[14:15], v36, v85
	v_cmp_ge_u32_e32 vcc, v5, v85
	v_addc_co_u32_e32 v86, vcc, 0, v86, vcc
	v_cmp_ge_u32_e64 s[16:17], v37, v85
	v_cmp_ge_u32_e32 vcc, v39, v85
	v_addc_co_u32_e32 v87, vcc, 0, v87, vcc
	v_cmp_ge_u32_e64 s[18:19], v67, v85
	v_cmp_ge_u32_e32 vcc, v38, v85
	v_addc_co_u32_e32 v86, vcc, 0, v86, vcc
	s_bcnt1_i32_b64 s13, s[14:15]
	s_add_i32 s12, s12, s13
	v_cmp_ge_u32_e64 s[20:21], v68, v85
	v_cmp_ge_u32_e32 vcc, v43, v85
	v_addc_co_u32_e32 v87, vcc, 0, v87, vcc
	s_bcnt1_i32_b64 s13, s[16:17]
	s_add_i32 s12, s12, s13
	v_cmp_ge_u32_e64 s[14:15], v69, v85
	s_bcnt1_i32_b64 s13, s[18:19]
	s_add_i32 s12, s12, s13
	v_cmp_ge_u32_e64 s[16:17], v73, v85
	v_cmp_ge_u32_e32 vcc, v70, v85
	v_addc_co_u32_e32 v86, vcc, 0, v86, vcc
	s_bcnt1_i32_b64 s13, s[20:21]
	s_add_i32 s12, s12, s13
	v_cmp_ge_u32_e64 s[18:19], v72, v85
	v_cmp_ge_u32_e32 vcc, v71, v85
	v_addc_co_u32_e32 v87, vcc, 0, v87, vcc
	s_bcnt1_i32_b64 s13, s[14:15]
	s_add_i32 s12, s12, s13
	v_cmp_ge_u32_e64 s[20:21], v52, v85
	v_cmp_ge_u32_e32 vcc, v74, v85
	v_addc_co_u32_e32 v86, vcc, 0, v86, vcc
	s_bcnt1_i32_b64 s13, s[16:17]
	s_add_i32 s12, s12, s13
	v_cmp_ge_u32_e64 s[14:15], v75, v85
	s_bcnt1_i32_b64 s13, s[18:19]
	s_add_i32 s12, s12, s13
	v_cmp_ge_u32_e64 s[16:17], v77, v85
	v_cmp_ge_u32_e32 vcc, v76, v85
	v_addc_co_u32_e32 v87, vcc, 0, v87, vcc
	s_bcnt1_i32_b64 s13, s[20:21]
	s_add_i32 s12, s12, s13
	v_cmp_ge_u32_e64 s[18:19], v78, v85
	v_cmp_ge_u32_e32 vcc, v80, v85
	v_addc_co_u32_e32 v86, vcc, 0, v86, vcc
	s_bcnt1_i32_b64 s13, s[14:15]
	s_add_i32 s12, s12, s13
	v_cmp_ge_u32_e64 s[20:21], v81, v85
	v_cmp_ge_u32_e32 vcc, v79, v85
	v_addc_co_u32_e32 v87, vcc, 0, v87, vcc
	s_bcnt1_i32_b64 s13, s[16:17]
	s_add_i32 s12, s12, s13
	v_cmp_ge_u32_e64 s[14:15], v82, v85
	v_cmp_ge_u32_e32 vcc, v62, v85
	v_addc_co_u32_e32 v86, vcc, 0, v86, vcc
	s_bcnt1_i32_b64 s13, s[18:19]
	s_add_i32 s12, s12, s13
	v_cmp_ge_u32_e64 s[16:17], v83, v85
	s_bcnt1_i32_b64 s13, s[20:21]
	s_add_i32 s12, s12, s13
	v_cmp_ge_u32_e64 s[18:19], v61, v85
	v_cmp_ge_u32_e32 vcc, v58, v85
	v_addc_co_u32_e32 v87, vcc, 0, v87, vcc
	s_bcnt1_i32_b64 s13, s[14:15]
	s_add_i32 s12, s12, s13
	v_cmp_ge_u32_e64 s[20:21], v60, v85
	v_cmp_ge_u32_e32 vcc, v59, v85
	v_addc_co_u32_e32 v86, vcc, 0, v86, vcc
	s_bcnt1_i32_b64 s13, s[16:17]
	s_add_i32 s12, s12, s13
	v_cmp_ge_u32_e64 s[14:15], v64, v85
	v_cmp_ge_u32_e32 vcc, v63, v85
	v_addc_co_u32_e32 v87, vcc, 0, v87, vcc
	s_bcnt1_i32_b64 s13, s[18:19]
	s_add_i32 s12, s12, s13
	v_cmp_ge_u32_e64 s[16:17], v65, v85
	s_bcnt1_i32_b64 s13, s[20:21]
	s_add_i32 s12, s12, s13
	s_bcnt1_i32_b64 s13, s[14:15]
	s_add_i32 s12, s12, s13
	s_bcnt1_i32_b64 s13, s[16:17]
	s_add_i32 s12, s12, s13
	v_add_u32_e32 v86, v87, v86
	v_and_b32_e32 v88, 1, v86
	v_cmp_ne_u32_e32 vcc, 0, v88
	s_bcnt1_i32_b64 s6, vcc
	v_bfe_u32 v88, v86, 1, 1
	v_cmp_ne_u32_e32 vcc, 0, v88
	s_bcnt1_i32_b64 s7, vcc
	s_lshl_b32 s7, s7, 1
	s_add_i32 s6, s6, s7
	v_bfe_u32 v88, v86, 2, 1
	v_cmp_ne_u32_e32 vcc, 0, v88
	s_bcnt1_i32_b64 s7, vcc
	s_lshl_b32 s7, s7, 2
	s_add_i32 s6, s6, s7
	v_bfe_u32 v88, v86, 3, 1
	v_cmp_ne_u32_e32 vcc, 0, v88
	s_bcnt1_i32_b64 s7, vcc
	s_lshl_b32 s7, s7, 3
	s_add_i32 s6, s6, s7
	s_add_i32 s8, s6, s12
	s_cmpk_eq_i32 s8, 0x100
	s_cselect_b64 s[6:7], -1, 0
	s_cmpk_lt_u32 s8, 0x100
	s_cselect_b64 vcc, -1, 0
	v_cndmask_b32_e32 v66, v85, v66, vcc
	v_subrev_co_u32_e32 v84, vcc, 1, v84
	s_or_b64 s[6:7], s[6:7], vcc
	s_andn2_b64 vcc, exec, s[6:7]
	s_cbranch_vccnz .LBB0_705
	s_branch .LBB0_712

; template <int NVM> __device__ __forceinline__ int cnt_ge(const unsigned (&key)[32], unsigned cand) {
;     unsigned c0 = 0, c1 = 0, c2 = 0, c3 = 0;
; #pragma unroll
;     for (int i = 0; i < NVM; i += 4) {
;         asm("v_cmp_ge_u32 vcc, %1, %2\n\tv_addc_co_u32 %0, vcc, 0, %0, vcc" : "+v"(c0) : "v"(key[i]), "v"(cand) : "vcc");
;         asm("v_cmp_ge_u32 vcc, %1, %2\n\tv_addc_co_u32 %0, vcc, 0, %0, vcc" : "+v"(c1) : "v"(key[i + 1]), "v"(cand) : "vcc");
;         asm("v_cmp_ge_u32 vcc, %1, %2\n\tv_addc_co_u32 %0, vcc, 0, %0, vcc" : "+v"(c2) : "v"(key[i + 2]), "v"(cand) : "vcc");
;         asm("v_cmp_ge_u32 vcc, %1, %2\n\tv_addc_co_u32 %0, vcc, 0, %0, vcc" : "+v"(c3) : "v"(key[i + 3]), "v"(cand) : "vcc"); }
;     const unsigned c = (c0 + c1) + (c2 + c3);
;     int tot = 0;
; #pragma unroll
;     for (int b = 0; b < 6; ++b) tot += __builtin_popcountll(__ballot((c >> b) & 1u)) << b;
;     return tot;
; }
; template <int NVM> __device__ __forceinline__ unsigned sel_thr(const unsigned (&key)[32]) {
;     unsigned Tt = 0u;
;     ...
;         if (cnt >= TOPK) { Tt = cand; if (cnt == TOPK) break; } }
;     return Tt;
; }
.LBB0_711:
	v_lshlrev_b32_e64 v78, v77, 1
	v_or_b32_e32 v78, v78, v66
	v_mov_b32_e32 v79, 0
	v_mov_b32_e32 v80, 0
	s_mov_b32 s12, 0
	v_cmp_ge_u32_e64 s[14:15], v36, v78
	v_cmp_ge_u32_e32 vcc, v5, v78
	v_addc_co_u32_e32 v79, vcc, 0, v79, vcc
	v_cmp_ge_u32_e64 s[16:17], v37, v78
	v_cmp_ge_u32_e32 vcc, v39, v78
	v_addc_co_u32_e32 v80, vcc, 0, v80, vcc
	v_cmp_ge_u32_e64 s[18:19], v67, v78
	v_cmp_ge_u32_e32 vcc, v38, v78
	v_addc_co_u32_e32 v79, vcc, 0, v79, vcc
	s_bcnt1_i32_b64 s13, s[14:15]
	s_add_i32 s12, s12, s13
	v_cmp_ge_u32_e64 s[20:21], v68, v78
	v_cmp_ge_u32_e32 vcc, v43, v78
	v_addc_co_u32_e32 v80, vcc, 0, v80, vcc
	s_bcnt1_i32_b64 s13, s[16:17]
	s_add_i32 s12, s12, s13
	v_cmp_ge_u32_e64 s[14:15], v70, v78
	v_cmp_ge_u32_e32 vcc, v69, v78
	v_addc_co_u32_e32 v79, vcc, 0, v79, vcc
	s_bcnt1_i32_b64 s13, s[18:19]
	s_add_i32 s12, s12, s13
	v_cmp_ge_u32_e64 s[16:17], v71, v78
	v_cmp_ge_u32_e32 vcc, v73, v78
	v_addc_co_u32_e32 v80, vcc, 0, v80, vcc
	s_bcnt1_i32_b64 s13, s[20:21]
	s_add_i32 s12, s12, s13
	v_cmp_ge_u32_e64 s[18:19], v72, v78
	s_bcnt1_i32_b64 s13, s[14:15]
	s_add_i32 s12, s12, s13
	v_cmp_ge_u32_e64 s[20:21], v52, v78
	v_cmp_ge_u32_e32 vcc, v74, v78
	v_addc_co_u32_e32 v79, vcc, 0, v79, vcc
	s_bcnt1_i32_b64 s13, s[16:17]
	s_add_i32 s12, s12, s13
	v_cmp_ge_u32_e64 s[14:15], v76, v78
	v_cmp_ge_u32_e32 vcc, v75, v78
	v_addc_co_u32_e32 v80, vcc, 0, v80, vcc
	s_bcnt1_i32_b64 s13, s[18:19]
	s_add_i32 s12, s12, s13
	v_cmp_ge_u32_e64 s[16:17], v54, v78
	v_cmp_ge_u32_e32 vcc, v50, v78
	v_addc_co_u32_e32 v79, vcc, 0, v79, vcc
	s_bcnt1_i32_b64 s13, s[20:21]
	s_add_i32 s12, s12, s13
	v_cmp_ge_u32_e64 s[18:19], v53, v78
	v_cmp_ge_u32_e32 vcc, v51, v78
	v_addc_co_u32_e32 v80, vcc, 0, v80, vcc
	s_bcnt1_i32_b64 s13, s[14:15]
	s_add_i32 s12, s12, s13
	v_cmp_ge_u32_e64 s[20:21], v56, v78
	v_cmp_ge_u32_e32 vcc, v55, v78
	v_addc_co_u32_e32 v79, vcc, 0, v79, vcc
	s_bcnt1_i32_b64 s13, s[16:17]
	s_add_i32 s12, s12, s13
	v_cmp_ge_u32_e64 s[14:15], v57, v78
	s_bcnt1_i32_b64 s13, s[18:19]
	s_add_i32 s12, s12, s13
	s_bcnt1_i32_b64 s13, s[20:21]
	s_add_i32 s12, s12, s13
	s_bcnt1_i32_b64 s13, s[14:15]
	s_add_i32 s12, s12, s13
	v_add_u32_e32 v79, v80, v79
	v_and_b32_e32 v81, 1, v79
	v_cmp_ne_u32_e32 vcc, 0, v81
	s_bcnt1_i32_b64 s6, vcc
	v_bfe_u32 v81, v79, 1, 1
	v_cmp_ne_u32_e32 vcc, 0, v81
	s_bcnt1_i32_b64 s7, vcc
	s_lshl_b32 s7, s7, 1
	s_add_i32 s6, s6, s7
	v_bfe_u32 v81, v79, 2, 1
	v_cmp_ne_u32_e32 vcc, 0, v81
	s_bcnt1_i32_b64 s7, vcc
	s_lshl_b32 s7, s7, 2
	s_add_i32 s6, s6, s7
	v_bfe_u32 v81, v79, 3, 1
	v_cmp_ne_u32_e32 vcc, 0, v81
	s_bcnt1_i32_b64 s7, vcc
	s_lshl_b32 s7, s7, 3
	s_add_i32 s6, s6, s7
	s_add_i32 s8, s6, s12
	s_cmpk_eq_i32 s8, 0x100
	s_cselect_b64 s[6:7], -1, 0
	s_cmpk_lt_u32 s8, 0x100
	s_cselect_b64 vcc, -1, 0
	v_cndmask_b32_e32 v66, v78, v66, vcc
	v_subrev_co_u32_e32 v77, vcc, 1, v77
	s_or_b64 s[6:7], s[6:7], vcc
	s_and_b64 vcc, exec, s[6:7]
	s_cbranch_vccz .LBB0_711

; template <int NVM> __device__ __forceinline__ int cnt_ge(const unsigned (&key)[32], unsigned cand) {
;     unsigned c0 = 0, c1 = 0, c2 = 0, c3 = 0;
; #pragma unroll
;     for (int i = 0; i < NVM; i += 4) {
;         asm("v_cmp_ge_u32 vcc, %1, %2\n\tv_addc_co_u32 %0, vcc, 0, %0, vcc" : "+v"(c0) : "v"(key[i]), "v"(cand) : "vcc");
;         asm("v_cmp_ge_u32 vcc, %1, %2\n\tv_addc_co_u32 %0, vcc, 0, %0, vcc" : "+v"(c1) : "v"(key[i + 1]), "v"(cand) : "vcc");
;         asm("v_cmp_ge_u32 vcc, %1, %2\n\tv_addc_co_u32 %0, vcc, 0, %0, vcc" : "+v"(c2) : "v"(key[i + 2]), "v"(cand) : "vcc");
;         asm("v_cmp_ge_u32 vcc, %1, %2\n\tv_addc_co_u32 %0, vcc, 0, %0, vcc" : "+v"(c3) : "v"(key[i + 3]), "v"(cand) : "vcc"); }
;     const unsigned c = (c0 + c1) + (c2 + c3);
;     int tot = 0;
; #pragma unroll
;     for (int b = 0; b < 6; ++b) tot += __builtin_popcountll(__ballot((c >> b) & 1u)) << b;
;     return tot;
; }
; template <int NVM> __device__ __forceinline__ unsigned sel_thr(const unsigned (&key)[32]) {
;     unsigned Tt = 0u;
;     ...
;         if (cnt >= TOPK) { Tt = cand; if (cnt == TOPK) break; } }
;     return Tt;
; }
.LBB0_714:
	v_lshlrev_b32_e64 v71, v70, 1
	v_or_b32_e32 v71, v71, v66
	v_mov_b32_e32 v72, 0
	v_mov_b32_e32 v73, 0
	s_mov_b32 s12, 0
	v_cmp_ge_u32_e64 s[14:15], v36, v71
	v_cmp_ge_u32_e32 vcc, v5, v71
	v_addc_co_u32_e32 v72, vcc, 0, v72, vcc
	v_cmp_ge_u32_e64 s[16:17], v37, v71
	v_cmp_ge_u32_e32 vcc, v39, v71
	v_addc_co_u32_e32 v73, vcc, 0, v73, vcc
	v_cmp_ge_u32_e64 s[18:19], v67, v71
	v_cmp_ge_u32_e32 vcc, v38, v71
	v_addc_co_u32_e32 v72, vcc, 0, v72, vcc
	s_bcnt1_i32_b64 s13, s[14:15]
	s_add_i32 s12, s12, s13
	v_cmp_ge_u32_e64 s[20:21], v68, v71
	v_cmp_ge_u32_e32 vcc, v43, v71
	v_addc_co_u32_e32 v73, vcc, 0, v73, vcc
	s_bcnt1_i32_b64 s13, s[16:17]
	s_add_i32 s12, s12, s13
	v_cmp_ge_u32_e64 s[14:15], v69, v71
	s_bcnt1_i32_b64 s13, s[18:19]
	s_add_i32 s12, s12, s13
	v_cmp_ge_u32_e64 s[16:17], v46, v71
	v_cmp_ge_u32_e32 vcc, v42, v71
	v_addc_co_u32_e32 v72, vcc, 0, v72, vcc
	s_bcnt1_i32_b64 s13, s[20:21]
	s_add_i32 s12, s12, s13
	v_cmp_ge_u32_e64 s[18:19], v45, v71
	v_cmp_ge_u32_e32 vcc, v44, v71
	v_addc_co_u32_e32 v73, vcc, 0, v73, vcc
	s_bcnt1_i32_b64 s13, s[14:15]
	s_add_i32 s12, s12, s13
	v_cmp_ge_u32_e64 s[20:21], v48, v71
	v_cmp_ge_u32_e32 vcc, v47, v71
	v_addc_co_u32_e32 v72, vcc, 0, v72, vcc
	s_bcnt1_i32_b64 s13, s[16:17]
	s_add_i32 s12, s12, s13
	v_cmp_ge_u32_e64 s[14:15], v49, v71
	s_bcnt1_i32_b64 s13, s[18:19]
	s_add_i32 s12, s12, s13
	s_bcnt1_i32_b64 s13, s[20:21]
	s_add_i32 s12, s12, s13
	s_bcnt1_i32_b64 s13, s[14:15]
	s_add_i32 s12, s12, s13
	v_add_u32_e32 v72, v73, v72
	v_and_b32_e32 v74, 1, v72
	v_cmp_ne_u32_e32 vcc, 0, v74
	s_bcnt1_i32_b64 s6, vcc
	v_bfe_u32 v74, v72, 1, 1
	v_cmp_ne_u32_e32 vcc, 0, v74
	s_bcnt1_i32_b64 s7, vcc
	s_lshl_b32 s7, s7, 1
	s_add_i32 s6, s6, s7
	v_bfe_u32 v74, v72, 2, 1
	v_cmp_ne_u32_e32 vcc, 0, v74
	s_bcnt1_i32_b64 s7, vcc
	s_lshl_b32 s7, s7, 2
	s_add_i32 s6, s6, s7
	s_add_i32 s8, s6, s12
	s_cmpk_eq_i32 s8, 0x100
	s_cselect_b64 s[6:7], -1, 0
	s_cmpk_lt_u32 s8, 0x100
	s_cselect_b64 vcc, -1, 0
	v_cndmask_b32_e32 v66, v71, v66, vcc
	v_subrev_co_u32_e32 v70, vcc, 1, v70
	s_or_b64 s[6:7], s[6:7], vcc
	s_and_b64 vcc, exec, s[6:7]
	s_cbranch_vccz .LBB0_714

; template <int NVM> __device__ __forceinline__ int cnt_ge(const unsigned (&key)[32], unsigned cand) {
;     unsigned c0 = 0, c1 = 0, c2 = 0, c3 = 0;
; #pragma unroll
;     for (int i = 0; i < NVM; i += 4) {
;         asm("v_cmp_ge_u32 vcc, %1, %2\n\tv_addc_co_u32 %0, vcc, 0, %0, vcc" : "+v"(c0) : "v"(key[i]), "v"(cand) : "vcc");
;         asm("v_cmp_ge_u32 vcc, %1, %2\n\tv_addc_co_u32 %0, vcc, 0, %0, vcc" : "+v"(c1) : "v"(key[i + 1]), "v"(cand) : "vcc");
;         asm("v_cmp_ge_u32 vcc, %1, %2\n\tv_addc_co_u32 %0, vcc, 0, %0, vcc" : "+v"(c2) : "v"(key[i + 2]), "v"(cand) : "vcc");
;         asm("v_cmp_ge_u32 vcc, %1, %2\n\tv_addc_co_u32 %0, vcc, 0, %0, vcc" : "+v"(c3) : "v"(key[i + 3]), "v"(cand) : "vcc"); }
;     const unsigned c = (c0 + c1) + (c2 + c3);
;     int tot = 0;
; #pragma unroll
;     for (int b = 0; b < 6; ++b) tot += __builtin_popcountll(__ballot((c >> b) & 1u)) << b;
;     return tot;
; }
; template <int NVM> __device__ __forceinline__ unsigned sel_thr(const unsigned (&key)[32]) {
;     unsigned Tt = 0u;
;     ...
;         if (cnt >= TOPK) { Tt = cand; if (cnt == TOPK) break; } }
;     return Tt;
; }
.LBB0_717:
	v_lshlrev_b32_e64 v68, v67, 1
	v_or_b32_e32 v68, v68, v66
	v_mov_b32_e32 v69, 0
	v_mov_b32_e32 v70, 0
	s_mov_b32 s12, 0
	v_cmp_ge_u32_e64 s[14:15], v36, v68
	v_cmp_ge_u32_e32 vcc, v5, v68
	v_addc_co_u32_e32 v69, vcc, 0, v69, vcc
	v_cmp_ge_u32_e64 s[16:17], v37, v68
	v_cmp_ge_u32_e32 vcc, v39, v68
	v_addc_co_u32_e32 v70, vcc, 0, v70, vcc
	v_cmp_ge_u32_e64 s[18:19], v35, v68
	v_cmp_ge_u32_e32 vcc, v38, v68
	v_addc_co_u32_e32 v69, vcc, 0, v69, vcc
	s_bcnt1_i32_b64 s13, s[14:15]
	s_add_i32 s12, s12, s13
	v_cmp_ge_u32_e64 s[20:21], v41, v68
	v_cmp_ge_u32_e32 vcc, v40, v68
	v_addc_co_u32_e32 v70, vcc, 0, v70, vcc
	s_bcnt1_i32_b64 s13, s[16:17]
	s_add_i32 s12, s12, s13
	s_bcnt1_i32_b64 s13, s[18:19]
	s_add_i32 s12, s12, s13
	s_bcnt1_i32_b64 s13, s[20:21]
	s_add_i32 s12, s12, s13
	v_add_u32_e32 v69, v70, v69
	v_and_b32_e32 v71, 1, v69
	v_cmp_ne_u32_e32 vcc, 0, v71
	s_bcnt1_i32_b64 s6, vcc
	v_bfe_u32 v71, v69, 1, 1
	v_cmp_ne_u32_e32 vcc, 0, v71
	s_bcnt1_i32_b64 s7, vcc
	s_lshl_b32 s7, s7, 1
	s_add_i32 s6, s6, s7
	v_bfe_u32 v71, v69, 2, 1
	v_cmp_ne_u32_e32 vcc, 0, v71
	s_bcnt1_i32_b64 s7, vcc
	s_lshl_b32 s7, s7, 2
	s_add_i32 s6, s6, s7
	s_add_i32 s8, s6, s12
	s_cmpk_eq_i32 s8, 0x100
	s_cselect_b64 s[6:7], -1, 0
	s_cmpk_lt_u32 s8, 0x100
	s_cselect_b64 vcc, -1, 0
	v_cndmask_b32_e32 v66, v68, v66, vcc
	v_subrev_co_u32_e32 v67, vcc, 1, v67
	s_or_b64 s[6:7], s[6:7], vcc
	s_and_b64 vcc, exec, s[6:7]
	s_cbranch_vccz .LBB0_717
